# baseline (speedup 1.0000x reference)
.LBB2_3:
	s_lshl_b32 s63, s53, 1
	s_add_i32 s61, s63, 2
	s_sub_i32 s2, s61, s40
	s_lshl_b32 s60, s53, 7
	s_min_i32 s62, s33, s2
	s_cmp_eq_u32 s55, 0
	s_cselect_b32 s79, 0, s62
	s_cmp_lt_i32 s2, 1
	s_waitcnt vmcnt(0)
	s_barrier
	s_cbranch_scc1 .LBB2_21
	s_add_i32 s63, s63, s55
	v_lshl_or_b32 v11, s63, 6, v83
	v_add_u32_e32 v10, s60, v82
	v_or_b32_e32 v12, 2, v11
	v_cmp_gt_i32_e64 s[6:7], v12, v10
	v_or_b32_e32 v12, 3, v11
	v_cmp_gt_i32_e64 s[8:9], v12, v10
	v_or_b32_e32 v12, 16, v11
	v_cmp_gt_i32_e64 s[10:11], v12, v10
	v_or_b32_e32 v12, 17, v11
	v_cmp_gt_i32_e64 s[12:13], v12, v10
	v_or_b32_e32 v12, 18, v11
	v_cmp_gt_i32_e64 s[14:15], v12, v10
	v_or_b32_e32 v12, 19, v11
	v_cmp_gt_i32_e64 s[16:17], v12, v10
	v_or_b32_e32 v12, 32, v11
	v_cmp_gt_i32_e64 s[18:19], v12, v10
	v_or_b32_e32 v12, 33, v11
	v_cmp_gt_i32_e64 s[20:21], v12, v10
	v_or_b32_e32 v12, 34, v11
	v_cmp_gt_i32_e64 s[22:23], v12, v10
	v_or_b32_e32 v12, 35, v11
	v_cmp_gt_i32_e64 s[24:25], v12, v10
	v_or_b32_e32 v12, 48, v11
	s_sub_i32 s37, s56, s40
	v_cmp_gt_i32_e64 s[26:27], v12, v10
	v_or_b32_e32 v12, 49, v11
	s_min_i32 s37, s33, s37
	v_cmp_gt_i32_e64 s[2:3], v11, v10
	v_cmp_lt_i32_e64 s[4:5], v11, v10
	v_cmp_gt_i32_e64 s[28:29], v12, v10
	v_or_b32_e32 v12, 50, v11
	v_or_b32_e32 v11, 51, v11
	s_max_i32 s37, s37, 1
	s_lshl_b64 s[38:39], s[40:41], 13
	v_mov_b32_e32 v67, 0
	v_cmp_gt_i32_e64 s[30:31], v12, v10
	v_cmp_gt_i32_e64 s[34:35], v11, v10
	s_mov_b32 s64, 1
	s_sub_i32 s65, 0, s37
	s_add_i32 s66, s40, s57
	s_add_u32 s68, s70, s38
	s_addc_u32 s69, s71, s39
	s_add_u32 s74, s72, s38
	s_addc_u32 s75, s73, s39
	v_mov_b32_e32 v14, v51
	v_mov_b32_e32 v15, v51
	v_mov_b32_e32 v16, v51
	v_mov_b32_e32 v17, v51
	s_mov_b64 s[38:39], -1
	v_mov_b32_e32 v30, 0
	v_mov_b32_e32 v31, v67
	v_mov_b32_e32 v32, v67
	v_mov_b32_e32 v33, v67
	v_mov_b32_e32 v26, 0
	v_mov_b32_e32 v27, v67
	v_mov_b32_e32 v28, v67
	v_mov_b32_e32 v29, v67
	v_mov_b32_e32 v22, v67
	v_mov_b32_e32 v23, v67
	v_mov_b32_e32 v24, v67
	v_mov_b32_e32 v25, v67
	v_mov_b32_e32 v18, v67
	v_mov_b32_e32 v19, v67
	v_mov_b32_e32 v20, v67
	v_mov_b32_e32 v21, v67
	v_mov_b32_e32 v10, v67
	v_mov_b32_e32 v11, v67
	v_mov_b32_e32 v12, v67
	v_mov_b32_e32 v13, v67
	s_mov_b32 s37, 0
	s_mov_b32 s80, 0
	s_mov_b32 s81, 0
	s_mov_b32 s48, s40
	v_mov_b32_e32 v114, v57
	v_mov_b32_e32 v115, v81
	v_mov_b32_e32 v120, v57
	v_mov_b32_e32 v121, v81
	s_cmp_gt_u32 s48, s63
	s_branch .Lattn_after_rdv
	.p2align 6
